# tail variant: tail WGs take only 2 DN units (DN units from round 2 on dealt to non-tail WGs)
# baseline (speedup 1.0000x reference)
; #define LAS __attribute__((address_space(3)))
;     __device__ __forceinline__ bool next(int i, Unit& u) const {
;         int U = i * G + c, e = 0, found = 0, rem = 0;
;         typedef int i32x4 __attribute__((ext_vector_type(4)));
;         const i32x4 c0 = *(const LAS i32x4*)(seg), c1 = *(const LAS i32x4*)(seg + 4), c2 = *(const LAS i32x4*)(seg + 8), c3 = *(const LAS i32x4*)(seg + 12);
; #pragma unroll
;         for (int k = 0; k < 16; ++k) { const int ck = k < 4 ? c0[k & 3] : k < 8 ? c1[k & 3] : k < 12 ? c2[k & 3] : c3[k & 3];
;             const int nu = ((ck + 255) >> 8) * nct; if (!found) { if (U < nu) { found = 1; e = k; rem = U; } else U -= nu; } }
;         if (!found) return false;
;         e = __builtin_amdgcn_readfirstlane(e); rem = __builtin_amdgcn_readfirstlane(rem);
;         const int rt = rem / nct, ct = rem % nct;
;         u.e = e; u.pm = rt; u.pn = ct; u.rows = seg[e] - rt * 256;
;         u.a = A + (size_t)(seg[16 + e] + rt * 256) * arow_bytes; u.b = Bt + (size_t)e * bexp_bytes + (size_t)ct * btile_bytes; return true;
;     __device__ __forceinline__ void pre(LAS unsigned char* lds, const pg8::Unit& u, int tid) const {
;         const int t = tid & 255, wv = __builtin_amdgcn_readfirstlane(tid >> 6);
;         const void* src = tid < 256 ? (const void*)(list + u.e * NTOK + u.pm * 256 + t) : (const void*)(listw + u.e * NTOK + u.pm * 256 + t);
;         lds_dma4(src, (unsigned)__builtin_amdgcn_readfirstlane((unsigned)(uintptr_t)lds + DNSL_OFF + u.par * 2048 + wv * 256));
;     }
.LBB0_1230:
	s_or_b64 exec, exec, s[24:25]
	s_lshl_b32 s8, s49, 11
	s_and_b32 s8, s8, 0x800
	s_lshl_b32 s9, s26, 2
	s_and_b32 s9, s9, 0xffffff00
	s_add_i32 s54, s8, 0
	s_add_i32 s8, s54, s9
	s_add_i32 s8, s8, 0x22400
	s_mov_b32 s9, m0
	s_mov_b32 m0, s8
	s_nop 0
	global_load_lds_dword v[36:37], off
	s_mov_b32 m0, s9
	v_mov_b32_e32 v34, s42
	ds_read_b128 v[134:137], v34
	s_add_i32 s23, s49, 1
	s_mul_i32 s8, s23, s77
	s_add_i32 s9, s8, s61
	s_cmp_lt_u32 s23, 2
	s_cbranch_scc1 .Ldn_perm_done
	v_readlane_b32 s24, v254, 63
	s_nop 1
	s_cmp_lt_u32 s61, s24
	s_cbranch_scc1 .Ldn_perm_bad
	s_sub_i32 s25, s77, s24
	s_add_i32 s26, s23, -2
	s_mul_i32 s25, s25, s26
	s_sub_i32 s26, s61, s24
	s_add_i32 s25, s25, s26
	s_lshl_b32 s26, s77, 1
	s_add_i32 s9, s25, s26
	s_lshl_b32 s26, s77, 2
	s_cmp_lt_u32 s9, s26
	s_cbranch_scc1 .Ldn_perm_done
	v_readlane_b32 s27, v254, 20
	s_nop 1
	s_lshl_b32 s27, s27, 2
	s_add_u32 s27, s27, 0x18000
	s_add_u32 s28, s92, s27
	s_addc_u32 s29, s93, 0
	v_mov_b32_e32 v138, 0
	s_mov_b32 s30, 0
